# v67 with the workgroups that take the down-projection-phase weight conversion chosen as c >= 3T (exactly those without a fifth-round unit for any expert-count draw) instead of c >= T+64
# baseline (speedup 1.0000x reference)
; #define LAS __attribute__((address_space(3)))
; __device__ __forceinline__ int opaque_tid() { int t = threadIdx.x; asm volatile("" : "+v"(t)); return t; }
;     const int tid = opaque_tid(), lane = tid & 63, wave = tid >> 6;
;     LAS float* scr = (LAS float*)(lds + 49152) + wave * (64 * 33);
;     const int gw = ((int)blockIdx.x - blk0) * NWAVES + wave, ngw = nblk * NWAVES;
;     constexpr int I_L = 16 * 104 + 16 * 32 + 16 * 16 * 32 + 16 * 8 * 32;
;     if ((int)blockIdx.x < blk0 || (int)blockIdx.x >= blk0 + nblk) return;
;     float tv[32];
;     const int I_E = it_hi < I_L ? it_hi : I_L;
;     int it = it_lo + gw;
;     if (it < I_E) { const PrepItem p = prep_decode(a, l, it);
; #pragma unroll
;         for (int i = 0; i < 32; ++i) tv[i] = __builtin_nontemporal_load(p.src + (size_t)(2 * i + (lane >> 5)) * p.ldw + (lane & 31)); }
; __device__ __forceinline__ void dn_mfma(const Args& a, LAS unsigned char* lds, int layer) {
;     seg_to_lds(a, lds, layer);
;     const LAS int* seg = (const LAS int*)(lds + SEG_OFF);
;     pg8::GroupedOrder So{(const char*)(a.ws + WS_HID), (const char*)(a.ws + WS_WDN + (size_t)layer * NE * 1024 * DFF * 2), seg, 4, (int)gridDim.x, (int)blockIdx.x, (size_t)DFF * 2, (size_t)1024 * DFF * 2, (size_t)256 * DFF * 2};
;     EpiDown E{(bf16_t*)(a.ws + WS_YBUF), (const int*)(a.ws + WS_LIST), (const float*)(a.ws + WS_LISTW), seg, lds};
;     pg8::gemm_phase<EpiDown, pg8::GroupedOrder>(lds, DFF, So, E);
; }
.LBB0_1321:
	v_readlane_b32 vcc_lo, v254, 16
	s_nop 1
	s_cmp_lg_u32 vcc_lo, 0
	s_cbranch_scc1 .Ldn_prep_skip
	v_readlane_b32 s4, v254, 63
	s_nop 1
	s_mul_i32 s4, s4, 3
	s_cmpk_eq_u32 s77, 0x100
	s_cselect_b32 s4, s4, 0
	s_sub_i32 s5, s77, s4
	s_cmp_ge_u32 s61, s4
	s_cselect_b64 s[6:7], -1, 0
	s_sub_i32 s8, s61, s4
	s_lshl_b32 s8, s8, 3
	s_addk_i32 s8, 0x2880
	s_lshl_b32 s5, s5, 3
	s_movk_i32 s9, 0x3880
	s_mov_b32 s10, 1
	s_nop 0
	v_writelane_b32 v252, s9, 36
	v_writelane_b32 v252, s5, 37
	v_writelane_b32 v252, s6, 38
	v_writelane_b32 v252, s7, 39
	v_writelane_b32 v252, s8, 40
	v_writelane_b32 v254, s10, 60
	v_mov_b32_e32 v112, v57
	s_mov_b64 s[44:45], -1
	s_branch .LBB0_302
